# phase 0: tile->job lookup by immediate compares (shape constants) instead of 9 dependent scalar loads, row-length load hoisted; plus router GEMM prefetch
# baseline (speedup 1.0000x reference)
.LBB0_33:
	s_or_b64 exec, exec, s[4:5]
	s_load_dword s3, s[0:1], 0x3a8
	s_waitcnt lgkmcnt(0)
	s_cmp_lt_i32 s2, s3
	s_cselect_b64 s[4:5], -1, 0
	s_cmp_ge_i32 s2, s3
	s_cbranch_scc1 .LBB0_45
	s_mov_b32 s10, 0
	s_cmp_lt_i32 s2, 0x1e0
	s_cselect_b32 s10, s10, 1
	s_cmp_lt_i32 s2, 0x200
	s_cselect_b32 s10, s10, 2
	s_cmp_lt_i32 s2, 0x220
	s_cselect_b32 s10, s10, 3
	s_cmp_lt_i32 s2, 0x240
	s_cselect_b32 s10, s10, 4
	s_cmp_lt_i32 s2, 0x2c0
	s_cselect_b32 s10, s10, 5
	s_cmp_lt_i32 s2, 0x5c0
	s_cselect_b32 s10, s10, 6
	s_cmp_lt_i32 s2, 0x9c0
	s_cselect_b32 s10, s10, 7
	s_cmp_lt_i32 s2, 0xbc0
	s_cselect_b32 s10, s10, 8
	s_cmp_lt_i32 s2, 0xcc0
	s_cselect_b32 s10, s10, 9
	s_mul_i32 s8, s10, 0x48
	s_mul_hi_u32 s9, s10, 0x48
	s_add_u32 s8, s0, s8
	s_addc_u32 s9, s1, s9
	s_load_dwordx2 s[10:11], s[8:9], 0xf8
	s_load_dword s14, s[8:9], 0x104
	s_load_dwordx2 s[12:13], s[8:9], 0xd8
	s_load_dword s16, s[8:9], 0xec
	v_mov_b32_e32 v7, 0
	v_mov_b32_e32 v8, v7
	s_waitcnt lgkmcnt(0)
	s_mul_i32 s11, s11, s10
	s_abs_i32 s15, s11
	v_cvt_f32_u32_e32 v0, s15
	s_sub_i32 s17, s2, s14
	s_xor_b32 s14, s17, s11
	s_ashr_i32 s19, s14, 31
	v_rcp_iflag_f32_e32 v0, v0
	s_sub_i32 s14, 0, s15
	s_abs_i32 s18, s17
	v_mov_b32_e32 v9, v7
	v_mul_f32_e32 v0, 0x4f7ffffe, v0
	v_cvt_u32_f32_e32 v0, v0
	s_nop 0
	v_readfirstlane_b32 s20, v0
	s_mul_i32 s14, s14, s20
	s_mul_hi_u32 s14, s20, s14
	s_add_i32 s20, s20, s14
	s_mul_hi_u32 s14, s18, s20
	s_mul_i32 s20, s14, s15
	s_sub_i32 s18, s18, s20
	s_add_i32 s21, s14, 1
	s_sub_i32 s20, s18, s15
	s_cmp_ge_u32 s18, s15
	s_cselect_b32 s14, s21, s14
	s_cselect_b32 s18, s20, s18
	s_add_i32 s20, s14, 1
	s_cmp_ge_u32 s18, s15
	s_cselect_b32 s18, s20, s14
	s_abs_i32 s20, s10
	v_cvt_f32_u32_e32 v0, s20
	s_xor_b32 s18, s18, s19
	s_sub_i32 s21, 0, s20
	s_sub_i32 s18, s18, s19
	v_rcp_iflag_f32_e32 v0, v0
	s_mul_i32 s11, s18, s11
	s_sub_i32 s11, s17, s11
	s_abs_i32 s19, s11
	v_mul_f32_e32 v0, 0x4f7ffffe, v0
	v_cvt_u32_f32_e32 v0, v0
	s_xor_b32 s17, s11, s10
	s_ashr_i32 s17, s17, 31
	s_load_dwordx2 s[14:15], s[8:9], 0x108
	s_load_dword s98, s[8:9], 0x118
	v_readfirstlane_b32 s22, v0
	s_mul_i32 s21, s21, s22
	s_mul_hi_u32 s21, s22, s21
	s_add_i32 s22, s22, s21
	s_mul_hi_u32 s21, s19, s22
	s_mul_i32 s22, s21, s20
	s_sub_i32 s19, s19, s22
	s_add_i32 s23, s21, 1
	s_sub_i32 s22, s19, s20
	s_cmp_ge_u32 s19, s20
	s_cselect_b32 s21, s23, s21
	s_cselect_b32 s19, s22, s19
	s_add_i32 s22, s21, 1
	s_cmp_ge_u32 s19, s20
	s_cselect_b32 s19, s22, s21
	s_xor_b32 s19, s19, s17
	s_sub_i32 s17, s19, s17
	s_mul_i32 s10, s17, s10
	s_sub_i32 s11, s11, s10
	s_lshl_b32 s10, s17, 7
	s_ashr_i32 s17, s18, 31
	s_waitcnt lgkmcnt(0)
	s_mul_i32 s17, s14, s17
	s_mul_hi_u32 s19, s14, s18
	s_add_i32 s17, s19, s17
	s_mul_i32 s15, s15, s18
	v_lshlrev_b32_e32 v0, 2, v250
	s_add_i32 s15, s17, s15
	s_mul_i32 s14, s14, s18
	v_and_b32_e32 v1, 0x7c, v0
	s_lshl_b64 s[14:15], s[14:15], 2
	v_or_b32_e32 v0, s10, v1
	s_add_u32 s12, s12, s14
	v_cmp_gt_i32_e32 vcc, s16, v0
	v_lshrrev_b32_e32 v0, 5, v250
	s_addc_u32 s13, s13, s15
	v_lshl_or_b32 v0, s11, 6, v0
	s_ashr_i32 s11, s10, 31
	s_lshl_b64 s[10:11], s[10:11], 2
	s_add_u32 s10, s12, s10
	s_addc_u32 s11, s13, s11
	v_lshlrev_b32_e32 v6, 2, v1
	v_lshl_add_u64 v[22:23], s[10:11], 0, v[6:7]
	v_mov_b32_e32 v6, v7
	v_mov_b64_e32 v[12:13], v[8:9]
	v_mov_b64_e32 v[10:11], v[6:7]
	s_and_saveexec_b64 s[10:11], vcc
	s_cbranch_execz .LBB0_38
	v_mad_i64_i32 v[2:3], s[12:13], s98, v0, 0
	v_lshl_add_u64 v[2:3], v[2:3], 2, v[22:23]
	global_load_dwordx4 v[10:13], v[2:3], off nt
.LBB0_38:
	s_or_b64 exec, exec, s[10:11]
	s_and_saveexec_b64 s[10:11], vcc
	s_cbranch_execz .LBB0_40
	v_add_u32_e32 v1, 16, v0
	v_mad_i64_i32 v[2:3], s[12:13], s98, v1, 0
	v_lshl_add_u64 v[2:3], v[2:3], 2, v[22:23]
	global_load_dwordx4 v[6:9], v[2:3], off nt
.LBB0_40:
	s_or_b64 exec, exec, s[10:11]
	v_mov_b32_e32 v2, 0
	v_mov_b32_e32 v4, v2
	v_mov_b32_e32 v5, v2
	v_mov_b32_e32 v3, v2
	v_mov_b64_e32 v[16:17], v[4:5]
	v_mov_b64_e32 v[14:15], v[2:3]
	s_and_saveexec_b64 s[10:11], vcc
	s_cbranch_execz .LBB0_42
	v_or_b32_e32 v1, 32, v0
	v_mad_i64_i32 v[4:5], s[12:13], s98, v1, 0
	v_lshl_add_u64 v[4:5], v[4:5], 2, v[22:23]
	global_load_dwordx4 v[14:17], v[4:5], off nt
.LBB0_42:
	s_or_b64 exec, exec, s[10:11]
	v_mov_b32_e32 v20, 0
	v_mov_b32_e32 v19, 0
	v_mov_b32_e32 v18, 0
	s_and_saveexec_b64 s[10:11], vcc
	s_cbranch_execz .LBB0_44
	v_add_u32_e32 v0, 48, v0
	v_mad_i64_i32 v[0:1], s[8:9], s98, v0, 0
	v_lshl_add_u64 v[0:1], v[0:1], 2, v[22:23]
	global_load_dwordx4 v[18:21], v[0:1], off nt
	s_waitcnt vmcnt(0)
	v_mov_b32_e32 v2, v21

.LBB0_49:
	s_and_b64 s[10:11], s[8:9], exec
	s_cselect_b32 s10, 0x8100, 0
	s_add_i32 s18, s10, 0
	s_add_i32 s18, s18, 0x10000
	v_add3_u32 v3, s18, v34, v31
	s_waitcnt lgkmcnt(0)
	v_add_u32_e32 v4, 0x2040, v3
	s_mov_b32 s19, s29
	s_waitcnt vmcnt(0)
	ds_write2_b32 v3, v10, v11 offset1:1
	ds_write2_b32 v3, v12, v13 offset0:2 offset1:3
	ds_write2_b32 v4, v6, v7 offset1:1
	v_add_u32_e32 v4, 0x2048, v3
	s_add_i32 s29, s29, s80
	ds_write2_b32 v4, v8, v9 offset1:1
	v_add_u32_e32 v4, 0x4080, v3
	s_cmp_ge_i32 s29, s3
	ds_write2_b32 v4, v14, v15 offset1:1
	v_add_u32_e32 v4, 0x4088, v3
	s_cselect_b64 s[10:11], -1, 0
	ds_write2_b32 v4, v16, v17 offset1:1
	v_add_u32_e32 v4, 0x60c0, v3
	v_add_u32_e32 v3, 0x60c8, v3
	s_and_b64 vcc, exec, s[10:11]
	ds_write2_b32 v4, v18, v19 offset1:1
	ds_write2_b32 v3, v20, v21 offset1:1
	s_waitcnt lgkmcnt(0)
	s_barrier
	s_cbranch_vccnz .LBB0_61
	s_mov_b32 s14, 0
	s_cmp_lt_i32 s29, 0x1e0
	s_cselect_b32 s14, s14, 1
	s_cmp_lt_i32 s29, 0x200
	s_cselect_b32 s14, s14, 2
	s_cmp_lt_i32 s29, 0x220
	s_cselect_b32 s14, s14, 3
	s_cmp_lt_i32 s29, 0x240
	s_cselect_b32 s14, s14, 4
	s_cmp_lt_i32 s29, 0x2c0
	s_cselect_b32 s14, s14, 5
	s_cmp_lt_i32 s29, 0x5c0
	s_cselect_b32 s14, s14, 6
	s_cmp_lt_i32 s29, 0x9c0
	s_cselect_b32 s14, s14, 7
	s_cmp_lt_i32 s29, 0xbc0
	s_cselect_b32 s14, s14, 8
	s_cmp_lt_i32 s29, 0xcc0
	s_cselect_b32 s14, s14, 9
	s_mul_i32 s12, s14, 0x48
	s_mul_hi_u32 s13, s14, 0x48
	s_add_u32 s12, s0, s12
	s_addc_u32 s13, s1, s13
	s_load_dwordx2 s[14:15], s[12:13], 0xf8
	s_load_dword s20, s[12:13], 0x104
	s_load_dwordx2 s[16:17], s[12:13], 0xd8
	s_load_dword s22, s[12:13], 0xec
	v_mov_b32_e32 v8, v2
	v_mov_b32_e32 v9, v2
	s_waitcnt lgkmcnt(0)
	s_mul_i32 s15, s15, s14
	s_abs_i32 s21, s15
	v_cvt_f32_u32_e32 v3, s21
	s_sub_i32 s23, s29, s20
	s_xor_b32 s20, s23, s15
	s_ashr_i32 s25, s20, 31
	v_rcp_iflag_f32_e32 v3, v3
	s_sub_i32 s20, 0, s21
	s_abs_i32 s24, s23
	v_mov_b32_e32 v35, v2
	v_mul_f32_e32 v3, 0x4f7ffffe, v3
	v_cvt_u32_f32_e32 v3, v3
	v_mov_b32_e32 v6, 0
	v_mov_b32_e32 v7, v2
	v_mov_b64_e32 v[12:13], v[8:9]
	v_readfirstlane_b32 s30, v3
	s_mul_i32 s20, s20, s30
	s_mul_hi_u32 s20, s30, s20
	s_add_i32 s30, s30, s20
	s_mul_hi_u32 s20, s24, s30
	s_mul_i32 s30, s20, s21
	s_sub_i32 s24, s24, s30
	s_add_i32 s31, s20, 1
	s_sub_i32 s30, s24, s21
	s_cmp_ge_u32 s24, s21
	s_cselect_b32 s20, s31, s20
	s_cselect_b32 s24, s30, s24
	s_add_i32 s30, s20, 1
	s_cmp_ge_u32 s24, s21
	s_cselect_b32 s24, s30, s20
	s_abs_i32 s30, s14
	v_cvt_f32_u32_e32 v3, s30
	s_xor_b32 s24, s24, s25
	s_sub_i32 s31, 0, s30
	s_sub_i32 s24, s24, s25
	v_rcp_iflag_f32_e32 v3, v3
	s_mul_i32 s15, s24, s15
	s_sub_i32 s15, s23, s15
	s_abs_i32 s25, s15
	v_mul_f32_e32 v3, 0x4f7ffffe, v3
	v_cvt_u32_f32_e32 v3, v3
	s_xor_b32 s23, s15, s14
	s_ashr_i32 s23, s23, 31
	s_load_dwordx2 s[20:21], s[12:13], 0x108
	s_load_dword s98, s[12:13], 0x118
	v_readfirstlane_b32 s34, v3
	s_mul_i32 s31, s31, s34
	s_mul_hi_u32 s31, s34, s31
	s_add_i32 s34, s34, s31
	s_mul_hi_u32 s31, s25, s34
	s_mul_i32 s34, s31, s30
	s_sub_i32 s25, s25, s34
	s_add_i32 s35, s31, 1
	s_sub_i32 s34, s25, s30
	s_cmp_ge_u32 s25, s30
	s_cselect_b32 s31, s35, s31
	s_cselect_b32 s25, s34, s25
	s_add_i32 s34, s31, 1
	s_cmp_ge_u32 s25, s30
	s_cselect_b32 s25, s34, s31
	s_xor_b32 s25, s25, s23
	s_sub_i32 s23, s25, s23
	s_mul_i32 s14, s23, s14
	s_sub_i32 s15, s15, s14
	s_lshl_b32 s14, s23, 7
	s_ashr_i32 s23, s24, 31
	s_waitcnt lgkmcnt(0)
	s_mul_i32 s23, s20, s23
	s_mul_hi_u32 s25, s20, s24
	s_add_i32 s23, s25, s23
	s_mul_i32 s21, s21, s24
	s_add_i32 s21, s23, s21
	s_mul_i32 s20, s20, s24
	s_lshl_b64 s[20:21], s[20:21], 2
	s_add_u32 s16, s16, s20
	s_addc_u32 s17, s17, s21
	v_lshl_or_b32 v24, s15, 6, v0
	s_ashr_i32 s15, s14, 31
	v_or_b32_e32 v3, s14, v30
	s_lshl_b64 s[14:15], s[14:15], 2
	s_add_u32 s14, s16, s14
	s_addc_u32 s15, s17, s15
	v_cmp_gt_i32_e32 vcc, s22, v3
	v_lshl_add_u64 v[22:23], s[14:15], 0, v[34:35]
	v_mov_b64_e32 v[10:11], v[6:7]
	s_and_saveexec_b64 s[14:15], vcc
	s_cbranch_execz .LBB0_54
	v_mad_i64_i32 v[4:5], s[16:17], s98, v24, 0
	v_lshl_add_u64 v[4:5], v[4:5], 2, v[22:23]
	global_load_dwordx4 v[10:13], v[4:5], off nt
.LBB0_54:
	s_or_b64 exec, exec, s[14:15]
	s_and_saveexec_b64 s[14:15], vcc
	s_cbranch_execz .LBB0_56
	v_add_u32_e32 v3, 16, v24
	v_mad_i64_i32 v[4:5], s[16:17], s98, v3, 0
	v_lshl_add_u64 v[4:5], v[4:5], 2, v[22:23]
	global_load_dwordx4 v[6:9], v[4:5], off nt
.LBB0_56:
	s_or_b64 exec, exec, s[14:15]
	v_mov_b32_e32 v4, v2
	v_mov_b32_e32 v5, v2
	v_mov_b32_e32 v3, v2
	v_mov_b64_e32 v[16:17], v[4:5]
	v_mov_b64_e32 v[14:15], v[2:3]
	s_and_saveexec_b64 s[14:15], vcc
	s_cbranch_execz .LBB0_58
	v_or_b32_e32 v3, 32, v24
	v_mad_i64_i32 v[4:5], s[16:17], s98, v3, 0
	v_lshl_add_u64 v[4:5], v[4:5], 2, v[22:23]
	global_load_dwordx4 v[14:17], v[4:5], off nt
.LBB0_58:
	s_or_b64 exec, exec, s[14:15]
	v_mov_b32_e32 v21, 0
	v_mov_b32_e32 v20, 0
	v_mov_b32_e32 v19, 0
	v_mov_b32_e32 v18, 0
	s_and_saveexec_b64 s[14:15], vcc
	s_cbranch_execz .LBB0_60
	v_add_u32_e32 v3, 48, v24
	v_mad_i64_i32 v[4:5], s[12:13], s98, v3, 0
	v_lshl_add_u64 v[4:5], v[4:5], 2, v[22:23]
	global_load_dwordx4 v[18:21], v[4:5], off nt

.LBB0_61:
	s_mov_b32 s14, 0
	s_cmp_lt_i32 s19, 0x1e0
	s_cselect_b32 s14, s14, 1
	s_cmp_lt_i32 s19, 0x200
	s_cselect_b32 s14, s14, 2
	s_cmp_lt_i32 s19, 0x220
	s_cselect_b32 s14, s14, 3
	s_cmp_lt_i32 s19, 0x240
	s_cselect_b32 s14, s14, 4
	s_cmp_lt_i32 s19, 0x2c0
	s_cselect_b32 s14, s14, 5
	s_cmp_lt_i32 s19, 0x5c0
	s_cselect_b32 s14, s14, 6
	s_cmp_lt_i32 s19, 0x9c0
	s_cselect_b32 s14, s14, 7
	s_cmp_lt_i32 s19, 0xbc0
	s_cselect_b32 s14, s14, 8
	s_cmp_lt_i32 s19, 0xcc0
	s_cselect_b32 s14, s14, 9
	s_mul_i32 s12, s14, 0x48
	s_mul_hi_u32 s13, s14, 0x48
	s_add_u32 s12, s0, s12
	s_addc_u32 s13, s1, s13
	s_load_dwordx2 s[16:17], s[12:13], 0xf8
	s_load_dword s14, s[12:13], 0x104
	s_waitcnt lgkmcnt(0)
	s_mul_i32 s15, s17, s16
	s_abs_i32 s17, s15
	v_cvt_f32_u32_e32 v3, s17
	s_sub_i32 s21, 0, s17
	s_sub_i32 s14, s19, s14
	s_abs_i32 s20, s14
	v_rcp_iflag_f32_e32 v3, v3
	s_xor_b32 s19, s14, s15
	s_ashr_i32 s19, s19, 31
	v_mul_f32_e32 v3, 0x4f7ffffe, v3
	v_cvt_u32_f32_e32 v3, v3
	s_nop 0
	v_readfirstlane_b32 s22, v3
	s_mul_i32 s21, s21, s22
	s_mul_hi_u32 s21, s22, s21
	s_add_i32 s22, s22, s21
	s_mul_hi_u32 s21, s20, s22
	s_mul_i32 s22, s21, s17
	s_sub_i32 s20, s20, s22
	s_add_i32 s23, s21, 1
	s_sub_i32 s22, s20, s17
	s_cmp_ge_u32 s20, s17
	s_cselect_b32 s21, s23, s21
	s_cselect_b32 s20, s22, s20
	s_add_i32 s22, s21, 1
	s_cmp_ge_u32 s20, s17
	s_cselect_b32 s17, s22, s21
	s_abs_i32 s20, s16
	v_cvt_f32_u32_e32 v3, s20
	s_xor_b32 s17, s17, s19
	s_sub_i32 s22, 0, s20
	s_sub_i32 s17, s17, s19
	v_rcp_iflag_f32_e32 v3, v3
	s_mul_i32 s15, s17, s15
	s_sub_i32 s19, s14, s15
	s_abs_i32 s15, s19
	v_mul_f32_e32 v3, 0x4f7ffffe, v3
	v_cvt_u32_f32_e32 v3, v3
	s_xor_b32 s14, s19, s16
	s_ashr_i32 s14, s14, 31
	s_load_dword s21, s[12:13], 0xec
	v_readfirstlane_b32 s23, v3
	s_mul_i32 s22, s22, s23
	s_mul_hi_u32 s22, s23, s22
	s_add_i32 s23, s23, s22
	s_mul_hi_u32 s22, s15, s23
	s_mul_i32 s23, s22, s20
	s_sub_i32 s15, s15, s23
	s_add_i32 s24, s22, 1
	s_sub_i32 s23, s15, s20
	s_cmp_ge_u32 s15, s20
	s_cselect_b32 s22, s24, s22
	s_cselect_b32 s15, s23, s15
	s_add_i32 s23, s22, 1
	s_cmp_ge_u32 s15, s20
	s_cselect_b32 s15, s23, s22
	s_xor_b32 s15, s15, s14
	s_sub_i32 s20, s15, s14
	v_lshl_or_b32 v3, s20, 7, v1
	s_waitcnt lgkmcnt(0)
	v_cmp_gt_i32_e32 vcc, s21, v3
	s_and_saveexec_b64 s[14:15], vcc
	s_cbranch_execz .LBB0_48
	s_mul_i32 s20, s20, s16
	v_lshlrev_b32_e32 v4, 2, v1
	s_sub_i32 s16, s19, s20
	s_load_dwordx2 s[20:21], s[12:13], 0x110
	v_add3_u32 v4, s18, v4, v42
	v_add_u32_e32 v5, 0x400, v4
	s_load_dwordx2 s[22:23], s[12:13], 0xe0
	s_load_dword s24, s[12:13], 0x11c
	ds_read2_b32 v[40:41], v5 offset0:2 offset1:131
	v_add_u32_e32 v5, 0x800, v4
	ds_read2_b32 v[24:25], v5 offset0:4 offset1:133
	v_add_u32_e32 v5, 0xc00, v4
	s_ashr_i32 s19, s17, 31
	ds_read2_b32 v[38:39], v5 offset0:6 offset1:135
	v_add_u32_e32 v5, 0x1000, v4
	s_waitcnt lgkmcnt(0)
	s_mul_hi_u32 s25, s20, s17
	s_mul_i32 s19, s20, s19
	ds_read2_b32 v[26:27], v5 offset0:8 offset1:137
	v_add_u32_e32 v5, 0x1400, v4
	s_add_i32 s19, s25, s19
	s_mul_i32 s21, s21, s17
	ds_read2_b32 v[22:23], v4 offset1:129
	ds_read2_b32 v[36:37], v5 offset0:10 offset1:139
	v_add_u32_e32 v5, 0x1800, v4
	v_add_u32_e32 v4, 0x1c00, v4
	s_add_i32 s21, s19, s21
	s_mul_i32 s20, s20, s17
	ds_read2_b32 v[28:29], v5 offset0:12 offset1:141
	ds_read2_b32 v[4:5], v4 offset0:14 offset1:143
	s_lshl_b32 s16, s16, 6
	s_lshl_b64 s[20:21], s[20:21], 1
	s_add_u32 s18, s22, s20
	s_addc_u32 s19, s23, s21
	s_cmp_eq_u32 s24, 0
	s_cbranch_scc1 .LBB0_66
	s_waitcnt lgkmcnt(3)
	v_mul_f32_e32 v35, 0x42800000, v22
	v_mul_f32_e32 v43, 0x42800000, v23
	v_mov_b32_e32 v44, v2
	v_cvt_pk_fp8_f32 v44, v35, v43
	v_mul_f32_e32 v35, 0x42800000, v40
	v_mul_f32_e32 v43, 0x42800000, v41
	v_mov_b32_e32 v45, v2
	v_cvt_pk_fp8_f32 v44, v35, v43 op_sel:[0,0,1]
	v_mul_f32_e32 v35, 0x42800000, v24
	v_mul_f32_e32 v43, 0x42800000, v25
	v_cvt_pk_fp8_f32 v45, v35, v43
	v_mul_f32_e32 v35, 0x42800000, v26
	v_mul_f32_e32 v43, 0x42800000, v27
	v_mov_b32_e32 v46, v2
	v_cvt_pk_fp8_f32 v46, v35, v43
	v_mul_f32_e32 v47, 0x42800000, v38
	v_mul_f32_e32 v48, 0x42800000, v39
	s_waitcnt lgkmcnt(2)
	v_mul_f32_e32 v35, 0x42800000, v36
	v_mul_f32_e32 v43, 0x42800000, v37
	v_cvt_pk_fp8_f32 v45, v47, v48 op_sel:[0,0,1]
	v_cvt_pk_fp8_f32 v46, v35, v43 op_sel:[0,0,1]
	s_waitcnt lgkmcnt(1)
	v_mul_f32_e32 v35, 0x42800000, v28
	v_mul_f32_e32 v43, 0x42800000, v29
	v_mov_b32_e32 v47, v2
	v_cvt_pk_fp8_f32 v47, v35, v43
	s_load_dword s17, s[12:13], 0xf0
	s_waitcnt lgkmcnt(0)
	v_mul_f32_e32 v35, 0x42800000, v4
	v_mul_f32_e32 v43, 0x42800000, v5
	v_cvt_pk_fp8_f32 v47, v35, v43 op_sel:[0,0,1]
	v_mov_b64_e32 v[48:49], s[18:19]
	v_mad_i64_i32 v[48:49], s[20:21], s17, v3, v[48:49]
	s_ashr_i32 s17, s16, 31
	v_lshl_add_u64 v[48:49], v[48:49], 0, s[16:17]
	v_lshl_add_u64 v[48:49], v[48:49], 0, v[32:33]
	global_store_dwordx4 v[48:49], v[44:47], off
	s_cbranch_execnz .LBB0_48
	s_branch .LBB0_67
